# stack: busy-workgroup shadow items at tail barriers, 3 items in up-GEMM tail, mixer-C refill DMA inside MFMA stream
# speedup vs baseline: 1.0036x; 1.0017x over previous
.Lcvt_t3:
	s_cmp_eq_u32 s31, 3
	s_cbranch_scc0 .Lcvt_t10
	s_mov_b32 s24, s62
	s_sub_i32 s27, s63, 208
	s_cmp_lt_i32 s27, 0
	s_cbranch_scc1 .Lcvt_t3b
	s_mov_b32 s26, 3
	s_movk_i32 s30, 5040
	s_movk_i32 s4, 6048
	s_branch .Lcvt_go
.Lcvt_t3b:
	s_mov_b32 s27, s63
	s_mov_b32 s26, 1
	s_movk_i32 s30, 6048
	s_movk_i32 s4, 7504
	s_branch .Lcvt_go
.Lcvt_t10:
	s_cmp_eq_u32 s31, 10
	s_cbranch_scc0 .Lcvt_lock
	s_cmp_ge_u32 s62, 3
	s_cbranch_scc1 .Lcvt_ret
	s_add_i32 s24, s62, 1
	s_sub_i32 s27, s63, 136
	s_cmp_lt_i32 s27, 0
	s_cbranch_scc1 .Lcvt_t10b
	s_mov_b32 s26, 4
	s_movk_i32 s30, 7504
	s_movk_i32 s4, 10864
	s_branch .Lcvt_go
.Lcvt_t10b:
	s_mov_b32 s27, s63
	s_mov_b32 s26, 1
	s_movk_i32 s30, 10864
	s_movk_i32 s4, 11816

.Lcvt_lk_c:
	s_mov_b32 s26, 2439
	s_mov_b32 s4, 17072
	s_cmp_eq_u32 s27, 1
	s_cselect_b32 s26, 1595, s26
	s_cselect_b32 s4, 12760, s4
	s_cmp_eq_u32 s27, 2
	s_cselect_b32 s26, 1595, s26
	s_cselect_b32 s4, 12760, s4
	s_cmp_eq_u32 s27, 3
	s_cselect_b32 s26, 2225, s26
	s_cselect_b32 s4, 17800, s4
	s_mul_i32 s30, s24, s26
	s_add_i32 s24, s30, s26
	s_min_u32 s4, s4, s24
	s_mul_i32 s26, s80, 7
	s_add_i32 s26, s26, s25
	s_add_i32 s26, s26, -1
	s_add_i32 s30, s30, s26
	s_mov_b32 s26, 2
	s_movk_i32 s25, 0x700
.Lcvt_item:
	s_cmp_ge_u32 s30, s4
	s_cbranch_scc1 .Lcvt_ret
	s_mov_b32 s6, s27
	s_mov_b32 s5, s30
	s_cmp_eq_u32 s25, 1
	s_cbranch_scc1 .Lcvt_dec
	s_cmp_eq_u32 s27, 3
	s_cbranch_scc1 .Lcvt_m3
	s_mov_b32 s24, 7504
	s_cmp_eq_u32 s27, 0
	s_cselect_b32 s24, s24, 11816
	s_add_i32 s5, s5, s24
	s_branch .Lcvt_dec
.Lcvt_m3:
	s_cmp_lt_u32 s5, 5040
	s_cbranch_scc1 .Lcvt_dec
	s_add_i32 s5, s5, 6776
